# fused LSTM: projection MFMA chain split across the pre-barrier and post-barrier idle windows; conflict-free xin LDS layout
# speedup vs baseline: 1.0070x; 1.0070x over previous
_Z12lstm2_kernelPKDF16_PKDv8_DF16_Pf:
	s_load_dwordx4 s[8:11], s[0:1], 0x0
	s_load_dwordx2 s[12:13], s[0:1], 0x10
	s_and_b32 s14, s2, 1
	s_lshr_b32 s15, s2, 1
	v_and_b32_e32 v1, 63, v0
	v_lshrrev_b32_e32 v2, 6, v0
	v_lshrrev_b32_e32 v3, 4, v1
	v_and_b32_e32 v4, 15, v0
	v_lshrrev_b32_e32 v5, 2, v4
	v_and_b32_e32 v6, 3, v0
	v_lshlrev_b32_e32 v7, 4, v1
	v_lshl_add_u32 v8, v2, 13, v7
	v_lshl_add_u32 v9, v2, 14, v7
	s_waitcnt lgkmcnt(0)
	s_lshl_b32 s16, s14, 15
	s_add_u32 s16, s16, 0x64000
	s_add_u32 s16, s10, s16
	s_addc_u32 s17, s11, 0
	s_lshl_b32 s18, s14, 16
	s_add_u32 s18, s18, 0x44000
	s_add_u32 s18, s10, s18
	s_addc_u32 s19, s11, 0
	v_add_u32_e32 v10, 0x1000, v8
	global_load_dwordx4 v[16:19], v8, s[16:17] offset:0
	global_load_dwordx4 v[20:23], v8, s[16:17] offset:1024
	global_load_dwordx4 v[24:27], v8, s[16:17] offset:2048
	global_load_dwordx4 v[28:31], v8, s[16:17] offset:3072
	global_load_dwordx4 v[32:35], v10, s[16:17] offset:0
	global_load_dwordx4 v[36:39], v10, s[16:17] offset:1024
	global_load_dwordx4 v[40:43], v10, s[16:17] offset:2048
	global_load_dwordx4 v[44:47], v10, s[16:17] offset:3072
	v_add_u32_e32 v11, 0x1000, v9
	v_add_u32_e32 v12, 0x2000, v9
	v_add_u32_e32 v13, 0x3000, v9
	global_load_dwordx4 v[48:51], v9, s[18:19] offset:0
	global_load_dwordx4 v[52:55], v9, s[18:19] offset:1024
	global_load_dwordx4 v[56:59], v9, s[18:19] offset:2048
	global_load_dwordx4 v[60:63], v9, s[18:19] offset:3072
	global_load_dwordx4 v[64:67], v11, s[18:19] offset:0
	global_load_dwordx4 v[68:71], v11, s[18:19] offset:1024
	global_load_dwordx4 v[72:75], v11, s[18:19] offset:2048
	global_load_dwordx4 v[76:79], v11, s[18:19] offset:3072
	global_load_dwordx4 v[80:83], v12, s[18:19] offset:0
	global_load_dwordx4 v[84:87], v12, s[18:19] offset:1024
	global_load_dwordx4 v[88:91], v12, s[18:19] offset:2048
	global_load_dwordx4 v[92:95], v12, s[18:19] offset:3072
	global_load_dwordx4 v[96:99], v13, s[18:19] offset:0
	global_load_dwordx4 v[100:103], v13, s[18:19] offset:1024
	global_load_dwordx4 v[104:107], v13, s[18:19] offset:2048
	global_load_dwordx4 v[108:111], v13, s[18:19] offset:3072
	s_lshl_b32 s22, s14, 10
	s_add_u32 s22, s8, s22
	s_addc_u32 s23, s9, 0
	v_lshl_add_u32 v14, v2, 4, v3
	v_lshlrev_b32_e32 v14, 2, v14
	global_load_dword v112, v14, s[22:23] offset:0
	global_load_dword v113, v14, s[22:23] offset:256
	global_load_dword v114, v14, s[22:23] offset:512
	global_load_dword v115, v14, s[22:23] offset:768
	global_load_dword v116, v14, s[22:23] offset:16
	global_load_dword v117, v14, s[22:23] offset:272
	global_load_dword v118, v14, s[22:23] offset:528
	global_load_dword v119, v14, s[22:23] offset:784
	global_load_dword v120, v14, s[22:23] offset:32
	global_load_dword v121, v14, s[22:23] offset:288
	global_load_dword v122, v14, s[22:23] offset:544
	global_load_dword v123, v14, s[22:23] offset:800
	global_load_dword v124, v14, s[22:23] offset:48
	global_load_dword v125, v14, s[22:23] offset:304
	global_load_dword v126, v14, s[22:23] offset:560
	global_load_dword v127, v14, s[22:23] offset:816
	s_add_u32 s24, s8, 0xc808000
	s_addc_u32 s25, s9, 0
	s_lshl_b32 s26, s15, 2
	v_add_u32_e32 v15, s26, v6
	s_cmp_eq_u32 s14, 0
	v_sub_u32_e32 v200, 0x18f, v5
	s_cselect_b64 vcc, -1, 0
	s_nop 1
	v_cndmask_b32_e32 v200, v200, v5, vcc
	v_mov_b32_e32 v201, 0x190
	v_mad_u32_u24 v200, v15, v201, v200
	v_lshlrev_b32_e32 v200, 8, v200
	v_lshl_add_u32 v200, v3, 4, v200
	v_mov_b32_e32 v201, 0
	v_lshl_add_u64 v[228:229], s[24:25], 0, v[200:201]
	s_mov_b32 s28, 0x400
	s_cselect_b32 s20, s28, 0xfffffc00
	s_cselect_b32 s21, 0, -1
	global_load_dwordx4 v[128:131], v[228:229], off offset:0
	global_load_dwordx4 v[132:135], v[228:229], off offset:64
	global_load_dwordx4 v[136:139], v[228:229], off offset:128
	global_load_dwordx4 v[140:143], v[228:229], off offset:192
	v_lshl_add_u64 v[228:229], v[228:229], 0, s[20:21]
	global_load_dwordx4 v[144:147], v[228:229], off offset:0
	global_load_dwordx4 v[148:151], v[228:229], off offset:64
	global_load_dwordx4 v[152:155], v[228:229], off offset:128
	global_load_dwordx4 v[156:159], v[228:229], off offset:192
	v_lshl_add_u64 v[228:229], v[228:229], 0, s[20:21]
	v_mul_u32_u24_e32 v202, 144, v6
	v_lshl_add_u32 v224, v3, 4, v202
	v_lshl_add_u32 v203, v2, 4, v3
	v_lshl_add_u32 v203, v5, 2, v203
	v_lshl_add_u32 v225, v203, 1, v202
	v_mul_u32_u24_e32 v204, 8704, v2
	v_lshlrev_b32_e32 v205, 8, v3
	v_lshl_add_u32 v205, v6, 4, v205
	v_add_u32_e32 v205, 1280, v205
	v_add_u32_e32 v205, v205, v204
	v_lshl_add_u32 v226, v5, 6, v205
	v_mul_u32_u24_e32 v206, 1088, v5
	v_add_u32_e32 v227, v205, v206
	s_lshl_b32 s27, s14, 6
	v_lshl_add_u32 v230, v15, 7, v203
	v_add_u32_e32 v230, s27, v230
	v_lshlrev_b32_e32 v230, 2, v230
	v_mov_b32_e32 v208, 0
	v_lshlrev_b32_e32 v209, 2, v0
	v_lshlrev_b32_e32 v210, 2, v1
	ds_write_b32 v209, v208
	ds_write_b32 v210, v208 offset:1024
	v_mov_b32_e32 v220, 0
	v_mov_b32_e32 v221, 0xff61b1e6
	v_mov_b32_e32 v222, 0x4038aa3b
	v_mov_b32_e32 v215, 0xff61b1e6
	s_waitcnt vmcnt(0)
	v_mfma_f32_16x16x32_f16 v[168:171], v[48:51], v[128:131], v[112:115]
	v_mfma_f32_16x16x32_f16 v[168:171], v[52:55], v[132:135], v[168:171]
	v_mfma_f32_16x16x32_f16 v[168:171], v[56:59], v[136:139], v[168:171]
	v_mfma_f32_16x16x32_f16 v[168:171], v[60:63], v[140:143], v[168:171]
	v_mfma_f32_16x16x32_f16 v[172:175], v[64:67], v[128:131], v[116:119]
	v_mfma_f32_16x16x32_f16 v[172:175], v[68:71], v[132:135], v[172:175]
	v_mfma_f32_16x16x32_f16 v[172:175], v[72:75], v[136:139], v[172:175]
	v_mfma_f32_16x16x32_f16 v[172:175], v[76:79], v[140:143], v[172:175]
	v_mfma_f32_16x16x32_f16 v[176:179], v[80:83], v[128:131], v[120:123]
	v_mfma_f32_16x16x32_f16 v[176:179], v[84:87], v[132:135], v[176:179]
	v_mfma_f32_16x16x32_f16 v[176:179], v[88:91], v[136:139], v[176:179]
	v_mfma_f32_16x16x32_f16 v[176:179], v[92:95], v[140:143], v[176:179]
	v_mfma_f32_16x16x32_f16 v[180:183], v[96:99], v[128:131], v[124:127]
	v_mfma_f32_16x16x32_f16 v[180:183], v[100:103], v[132:135], v[180:183]
	v_mfma_f32_16x16x32_f16 v[180:183], v[104:107], v[136:139], v[180:183]
	v_mfma_f32_16x16x32_f16 v[180:183], v[108:111], v[140:143], v[180:183]
	v_mfma_f32_16x16x32_f16 v[160:163], v[48:51], v[144:147], v[112:115]
	v_mfma_f32_16x16x32_f16 v[160:163], v[52:55], v[148:151], v[160:163]
	s_nop 7
	ds_write_b128 v227, v[168:171] offset:0
	ds_write_b128 v227, v[172:175] offset:64
	ds_write_b128 v227, v[176:179] offset:128
	ds_write_b128 v227, v[180:183] offset:192
	s_movk_i32 s4, 50
	s_waitcnt lgkmcnt(0)
	s_barrier
	ds_read_b128 v[192:195], v226 offset:0
.Llstm3_loop:
	ds_read_b128 v[184:187], v224 offset:0
	ds_read_b128 v[188:191], v224 offset:64
	v_mfma_f32_16x16x32_f16 v[160:163], v[56:59], v[152:155], v[160:163]
	v_mfma_f32_16x16x32_f16 v[160:163], v[60:63], v[156:159], v[160:163]
	global_load_dwordx4 v[128:131], v[228:229], off offset:0
	global_load_dwordx4 v[132:135], v[228:229], off offset:64
	global_load_dwordx4 v[136:139], v[228:229], off offset:128
	global_load_dwordx4 v[140:143], v[228:229], off offset:192
	v_lshl_add_u64 v[228:229], v[228:229], 0, s[20:21]
	s_waitcnt lgkmcnt(0)
	v_mfma_f32_16x16x32_f16 v[168:171], v[16:19], v[184:187], v[192:195]
	v_mfma_f32_16x16x32_f16 v[172:175], v[24:27], v[184:187], v[192:195]
	v_mfma_f32_16x16x32_f16 v[176:179], v[32:35], v[184:187], v[192:195]
	v_mfma_f32_16x16x32_f16 v[180:183], v[40:43], v[184:187], v[192:195]
	v_mfma_f32_16x16x32_f16 v[168:171], v[20:23], v[188:191], v[168:171]
	v_mfma_f32_16x16x32_f16 v[172:175], v[28:31], v[188:191], v[172:175]
	v_mfma_f32_16x16x32_f16 v[176:179], v[36:39], v[188:191], v[176:179]
	v_max_f32_e32 v221, v221, v215
	s_nop 5
	v_mov_b32_dpp v168, v172 quad_perm:[0,1,2,3] row_mask:0xf bank_mask:0x2
	v_mov_b32_dpp v169, v173 quad_perm:[0,1,2,3] row_mask:0xf bank_mask:0x2
	v_mfma_f32_16x16x32_f16 v[180:183], v[44:47], v[188:191], v[180:183]
	v_mov_b32_dpp v170, v174 quad_perm:[0,1,2,3] row_mask:0xf bank_mask:0x2
	v_mov_b32_dpp v171, v175 quad_perm:[0,1,2,3] row_mask:0xf bank_mask:0x2
	s_nop 5
	v_mov_b32_dpp v176, v180 quad_perm:[0,1,2,3] row_mask:0xf bank_mask:0x8
	v_mov_b32_dpp v177, v181 quad_perm:[0,1,2,3] row_mask:0xf bank_mask:0x8
	v_mov_b32_dpp v178, v182 quad_perm:[0,1,2,3] row_mask:0xf bank_mask:0x8
	v_mov_b32_dpp v168, v176 quad_perm:[0,1,2,3] row_mask:0xf bank_mask:0xc
	v_mov_b32_dpp v169, v177 quad_perm:[0,1,2,3] row_mask:0xf bank_mask:0xc
	v_exp_f32_e32 v200, v168
	v_mov_b32_dpp v170, v178 quad_perm:[0,1,2,3] row_mask:0xf bank_mask:0xc
	v_exp_f32_e32 v201, v169
	v_mov_b32_dpp v179, v183 quad_perm:[0,1,2,3] row_mask:0xf bank_mask:0x8
	v_exp_f32_e32 v202, v170
	v_add_f32_e32 v200, 1.0, v200
	v_add_f32_e32 v201, 1.0, v201
	v_mov_b32_dpp v171, v179 quad_perm:[0,1,2,3] row_mask:0xf bank_mask:0xc
	v_add_f32_e32 v202, 1.0, v202
	v_rcp_f32_e32 v202, v202
	v_exp_f32_e32 v203, v171
	v_rcp_f32_e32 v200, v200
	v_rcp_f32_e32 v201, v201
	v_fmamk_f32 v204, v202, 0xc0b8aa3b, v222
	v_add_f32_e32 v203, 1.0, v203
	v_mul_f32_e32 v205, v200, v204
	v_rcp_f32_e32 v203, v203
	v_fma_f32 v220, v201, v220, v205
	v_exp_f32_e32 v206, v220
	v_mul_f32_e32 v207, -2.0, v203
	v_add_f32_e32 v206, 1.0, v206
	v_rcp_f32_e32 v206, v206
	s_nop 0
	v_fma_mixlo_f16 v208, v206, v207, v203
	ds_write_b16 v225, v208 offset:576
	ds_write_b128 v227, v[160:163] offset:4352
	ds_read_b128 v[196:199], v226 offset:1088
	v_fma_f32 v215, v206, v207, v203
	v_mfma_f32_16x16x32_f16 v[164:167], v[64:67], v[144:147], v[116:119]
	v_mfma_f32_16x16x32_f16 v[164:167], v[68:71], v[148:151], v[164:167]
	s_waitcnt lgkmcnt(1)
	s_barrier
	ds_read_b128 v[184:187], v224 offset:576
	ds_read_b128 v[188:191], v224 offset:640
	v_mfma_f32_16x16x32_f16 v[164:167], v[72:75], v[152:155], v[164:167]
	v_mfma_f32_16x16x32_f16 v[164:167], v[76:79], v[156:159], v[164:167]
	s_waitcnt lgkmcnt(0)
	v_mfma_f32_16x16x32_f16 v[168:171], v[16:19], v[184:187], v[196:199]
	v_mfma_f32_16x16x32_f16 v[172:175], v[24:27], v[184:187], v[196:199]
	v_mfma_f32_16x16x32_f16 v[176:179], v[32:35], v[184:187], v[196:199]
	v_mfma_f32_16x16x32_f16 v[180:183], v[40:43], v[184:187], v[196:199]
	v_mfma_f32_16x16x32_f16 v[168:171], v[20:23], v[188:191], v[168:171]
	v_mfma_f32_16x16x32_f16 v[172:175], v[28:31], v[188:191], v[172:175]
	v_mfma_f32_16x16x32_f16 v[176:179], v[36:39], v[188:191], v[176:179]
	v_max_f32_e32 v221, v221, v215
	s_nop 5
	v_mov_b32_dpp v168, v172 quad_perm:[0,1,2,3] row_mask:0xf bank_mask:0x2
	v_mov_b32_dpp v169, v173 quad_perm:[0,1,2,3] row_mask:0xf bank_mask:0x2
	v_mfma_f32_16x16x32_f16 v[180:183], v[44:47], v[188:191], v[180:183]
	v_mov_b32_dpp v170, v174 quad_perm:[0,1,2,3] row_mask:0xf bank_mask:0x2
	v_mov_b32_dpp v171, v175 quad_perm:[0,1,2,3] row_mask:0xf bank_mask:0x2
	s_nop 5
	v_mov_b32_dpp v176, v180 quad_perm:[0,1,2,3] row_mask:0xf bank_mask:0x8
	v_mov_b32_dpp v177, v181 quad_perm:[0,1,2,3] row_mask:0xf bank_mask:0x8
	v_mov_b32_dpp v178, v182 quad_perm:[0,1,2,3] row_mask:0xf bank_mask:0x8
	v_mov_b32_dpp v168, v176 quad_perm:[0,1,2,3] row_mask:0xf bank_mask:0xc
	v_mov_b32_dpp v169, v177 quad_perm:[0,1,2,3] row_mask:0xf bank_mask:0xc
	v_exp_f32_e32 v200, v168
	v_mov_b32_dpp v170, v178 quad_perm:[0,1,2,3] row_mask:0xf bank_mask:0xc
	v_exp_f32_e32 v201, v169
	v_mov_b32_dpp v179, v183 quad_perm:[0,1,2,3] row_mask:0xf bank_mask:0x8
	v_exp_f32_e32 v202, v170
	v_add_f32_e32 v200, 1.0, v200
	v_add_f32_e32 v201, 1.0, v201
	v_mov_b32_dpp v171, v179 quad_perm:[0,1,2,3] row_mask:0xf bank_mask:0xc
	v_add_f32_e32 v202, 1.0, v202
	v_rcp_f32_e32 v202, v202
	v_exp_f32_e32 v203, v171
	v_rcp_f32_e32 v200, v200
	v_rcp_f32_e32 v201, v201
	v_fmamk_f32 v204, v202, 0xc0b8aa3b, v222
	v_add_f32_e32 v203, 1.0, v203
	v_mul_f32_e32 v205, v200, v204
	v_rcp_f32_e32 v203, v203
	v_fma_f32 v220, v201, v220, v205
	v_exp_f32_e32 v206, v220
	v_mul_f32_e32 v207, -2.0, v203
	v_add_f32_e32 v206, 1.0, v206
	v_rcp_f32_e32 v206, v206
	s_nop 0
	v_fma_mixlo_f16 v208, v206, v207, v203
	ds_write_b16 v225, v208 offset:0
	ds_write_b128 v227, v[164:167] offset:4416
	ds_read_b128 v[192:195], v226 offset:2176
	v_fma_f32 v215, v206, v207, v203
	v_mfma_f32_16x16x32_f16 v[160:163], v[80:83], v[144:147], v[120:123]
	v_mfma_f32_16x16x32_f16 v[160:163], v[84:87], v[148:151], v[160:163]
	s_waitcnt lgkmcnt(1)
	s_barrier
	ds_read_b128 v[184:187], v224 offset:0
	ds_read_b128 v[188:191], v224 offset:64
	v_mfma_f32_16x16x32_f16 v[160:163], v[88:91], v[152:155], v[160:163]
	v_mfma_f32_16x16x32_f16 v[160:163], v[92:95], v[156:159], v[160:163]
	s_waitcnt lgkmcnt(0)
	v_mfma_f32_16x16x32_f16 v[168:171], v[16:19], v[184:187], v[192:195]
	v_mfma_f32_16x16x32_f16 v[172:175], v[24:27], v[184:187], v[192:195]
	v_mfma_f32_16x16x32_f16 v[176:179], v[32:35], v[184:187], v[192:195]
	v_mfma_f32_16x16x32_f16 v[180:183], v[40:43], v[184:187], v[192:195]
	v_mfma_f32_16x16x32_f16 v[168:171], v[20:23], v[188:191], v[168:171]
	v_mfma_f32_16x16x32_f16 v[172:175], v[28:31], v[188:191], v[172:175]
	v_mfma_f32_16x16x32_f16 v[176:179], v[36:39], v[188:191], v[176:179]
	v_max_f32_e32 v221, v221, v215
	s_nop 5
	v_mov_b32_dpp v168, v172 quad_perm:[0,1,2,3] row_mask:0xf bank_mask:0x2
	v_mov_b32_dpp v169, v173 quad_perm:[0,1,2,3] row_mask:0xf bank_mask:0x2
	v_mfma_f32_16x16x32_f16 v[180:183], v[44:47], v[188:191], v[180:183]
	v_mov_b32_dpp v170, v174 quad_perm:[0,1,2,3] row_mask:0xf bank_mask:0x2
	v_mov_b32_dpp v171, v175 quad_perm:[0,1,2,3] row_mask:0xf bank_mask:0x2
	s_nop 5
	v_mov_b32_dpp v176, v180 quad_perm:[0,1,2,3] row_mask:0xf bank_mask:0x8
	v_mov_b32_dpp v177, v181 quad_perm:[0,1,2,3] row_mask:0xf bank_mask:0x8
	v_mov_b32_dpp v178, v182 quad_perm:[0,1,2,3] row_mask:0xf bank_mask:0x8
	v_mov_b32_dpp v168, v176 quad_perm:[0,1,2,3] row_mask:0xf bank_mask:0xc
	v_mov_b32_dpp v169, v177 quad_perm:[0,1,2,3] row_mask:0xf bank_mask:0xc
	v_exp_f32_e32 v200, v168
	v_mov_b32_dpp v170, v178 quad_perm:[0,1,2,3] row_mask:0xf bank_mask:0xc
	v_exp_f32_e32 v201, v169
	v_mov_b32_dpp v179, v183 quad_perm:[0,1,2,3] row_mask:0xf bank_mask:0x8
	v_exp_f32_e32 v202, v170
	v_add_f32_e32 v200, 1.0, v200
	v_add_f32_e32 v201, 1.0, v201
	v_mov_b32_dpp v171, v179 quad_perm:[0,1,2,3] row_mask:0xf bank_mask:0xc
	v_add_f32_e32 v202, 1.0, v202
	v_rcp_f32_e32 v202, v202
	v_exp_f32_e32 v203, v171
	v_rcp_f32_e32 v200, v200
	v_rcp_f32_e32 v201, v201
	v_fmamk_f32 v204, v202, 0xc0b8aa3b, v222
	v_add_f32_e32 v203, 1.0, v203
	v_mul_f32_e32 v205, v200, v204
	v_rcp_f32_e32 v203, v203
	v_fma_f32 v220, v201, v220, v205
	v_exp_f32_e32 v206, v220
	v_mul_f32_e32 v207, -2.0, v203
	v_add_f32_e32 v206, 1.0, v206
	v_rcp_f32_e32 v206, v206
	s_nop 0
	v_fma_mixlo_f16 v208, v206, v207, v203
	ds_write_b16 v225, v208 offset:576
	ds_write_b128 v227, v[160:163] offset:4480
	ds_read_b128 v[196:199], v226 offset:3264
	v_fma_f32 v215, v206, v207, v203
	v_mfma_f32_16x16x32_f16 v[164:167], v[96:99], v[144:147], v[124:127]
	v_mfma_f32_16x16x32_f16 v[164:167], v[100:103], v[148:151], v[164:167]
	s_waitcnt lgkmcnt(1)
	s_barrier
	ds_read_b128 v[184:187], v224 offset:576
	ds_read_b128 v[188:191], v224 offset:640
	v_mfma_f32_16x16x32_f16 v[164:167], v[104:107], v[152:155], v[164:167]
	v_mfma_f32_16x16x32_f16 v[164:167], v[108:111], v[156:159], v[164:167]
	s_waitcnt lgkmcnt(0)
	v_mfma_f32_16x16x32_f16 v[168:171], v[16:19], v[184:187], v[196:199]
	v_mfma_f32_16x16x32_f16 v[172:175], v[24:27], v[184:187], v[196:199]
	v_mfma_f32_16x16x32_f16 v[176:179], v[32:35], v[184:187], v[196:199]
	v_mfma_f32_16x16x32_f16 v[180:183], v[40:43], v[184:187], v[196:199]
	v_mfma_f32_16x16x32_f16 v[168:171], v[20:23], v[188:191], v[168:171]
	v_mfma_f32_16x16x32_f16 v[172:175], v[28:31], v[188:191], v[172:175]
	v_mfma_f32_16x16x32_f16 v[176:179], v[36:39], v[188:191], v[176:179]
	v_max_f32_e32 v221, v221, v215
	s_nop 5
	v_mov_b32_dpp v168, v172 quad_perm:[0,1,2,3] row_mask:0xf bank_mask:0x2
	v_mov_b32_dpp v169, v173 quad_perm:[0,1,2,3] row_mask:0xf bank_mask:0x2
	v_mfma_f32_16x16x32_f16 v[180:183], v[44:47], v[188:191], v[180:183]
	v_mov_b32_dpp v170, v174 quad_perm:[0,1,2,3] row_mask:0xf bank_mask:0x2
	v_mov_b32_dpp v171, v175 quad_perm:[0,1,2,3] row_mask:0xf bank_mask:0x2
	s_nop 5
	v_mov_b32_dpp v176, v180 quad_perm:[0,1,2,3] row_mask:0xf bank_mask:0x8
	v_mov_b32_dpp v177, v181 quad_perm:[0,1,2,3] row_mask:0xf bank_mask:0x8
	v_mov_b32_dpp v178, v182 quad_perm:[0,1,2,3] row_mask:0xf bank_mask:0x8
	v_mov_b32_dpp v168, v176 quad_perm:[0,1,2,3] row_mask:0xf bank_mask:0xc
	v_mov_b32_dpp v169, v177 quad_perm:[0,1,2,3] row_mask:0xf bank_mask:0xc
	v_exp_f32_e32 v200, v168
	v_mov_b32_dpp v170, v178 quad_perm:[0,1,2,3] row_mask:0xf bank_mask:0xc
	v_exp_f32_e32 v201, v169
	v_mov_b32_dpp v179, v183 quad_perm:[0,1,2,3] row_mask:0xf bank_mask:0x8
	v_exp_f32_e32 v202, v170
	v_add_f32_e32 v200, 1.0, v200
	v_add_f32_e32 v201, 1.0, v201
	v_mov_b32_dpp v171, v179 quad_perm:[0,1,2,3] row_mask:0xf bank_mask:0xc
	v_add_f32_e32 v202, 1.0, v202
	v_rcp_f32_e32 v202, v202
	v_exp_f32_e32 v203, v171
	v_rcp_f32_e32 v200, v200
	v_rcp_f32_e32 v201, v201
	v_fmamk_f32 v204, v202, 0xc0b8aa3b, v222
	v_add_f32_e32 v203, 1.0, v203
	v_mul_f32_e32 v205, v200, v204
	v_rcp_f32_e32 v203, v203
	v_fma_f32 v220, v201, v220, v205
	v_exp_f32_e32 v206, v220
	v_mul_f32_e32 v207, -2.0, v203
	v_add_f32_e32 v206, 1.0, v206
	v_rcp_f32_e32 v206, v206
	s_nop 0
	v_fma_mixlo_f16 v208, v206, v207, v203
	ds_write_b16 v225, v208 offset:0
	ds_write_b128 v227, v[164:167] offset:4544
	ds_read_b128 v[192:195], v226 offset:4352
	v_fma_f32 v215, v206, v207, v203
	s_waitcnt vmcnt(0)
	v_mfma_f32_16x16x32_f16 v[160:163], v[48:51], v[128:131], v[112:115]
	v_mfma_f32_16x16x32_f16 v[160:163], v[52:55], v[132:135], v[160:163]
	s_waitcnt lgkmcnt(1)
	s_barrier
	ds_read_b128 v[184:187], v224 offset:0
	ds_read_b128 v[188:191], v224 offset:64
	v_mfma_f32_16x16x32_f16 v[160:163], v[56:59], v[136:139], v[160:163]
	v_mfma_f32_16x16x32_f16 v[160:163], v[60:63], v[140:143], v[160:163]
	global_load_dwordx4 v[144:147], v[228:229], off offset:0
	global_load_dwordx4 v[148:151], v[228:229], off offset:64
	global_load_dwordx4 v[152:155], v[228:229], off offset:128
	global_load_dwordx4 v[156:159], v[228:229], off offset:192
	v_lshl_add_u64 v[228:229], v[228:229], 0, s[20:21]
	s_waitcnt lgkmcnt(0)
	v_mfma_f32_16x16x32_f16 v[168:171], v[16:19], v[184:187], v[192:195]
	v_mfma_f32_16x16x32_f16 v[172:175], v[24:27], v[184:187], v[192:195]
	v_mfma_f32_16x16x32_f16 v[176:179], v[32:35], v[184:187], v[192:195]
	v_mfma_f32_16x16x32_f16 v[180:183], v[40:43], v[184:187], v[192:195]
	v_mfma_f32_16x16x32_f16 v[168:171], v[20:23], v[188:191], v[168:171]
	v_mfma_f32_16x16x32_f16 v[172:175], v[28:31], v[188:191], v[172:175]
	v_mfma_f32_16x16x32_f16 v[176:179], v[36:39], v[188:191], v[176:179]
	v_max_f32_e32 v221, v221, v215
	s_nop 5
	v_mov_b32_dpp v168, v172 quad_perm:[0,1,2,3] row_mask:0xf bank_mask:0x2
	v_mov_b32_dpp v169, v173 quad_perm:[0,1,2,3] row_mask:0xf bank_mask:0x2
	v_mfma_f32_16x16x32_f16 v[180:183], v[44:47], v[188:191], v[180:183]
	v_mov_b32_dpp v170, v174 quad_perm:[0,1,2,3] row_mask:0xf bank_mask:0x2
	v_mov_b32_dpp v171, v175 quad_perm:[0,1,2,3] row_mask:0xf bank_mask:0x2
	s_nop 5
	v_mov_b32_dpp v176, v180 quad_perm:[0,1,2,3] row_mask:0xf bank_mask:0x8
	v_mov_b32_dpp v177, v181 quad_perm:[0,1,2,3] row_mask:0xf bank_mask:0x8
	v_mov_b32_dpp v178, v182 quad_perm:[0,1,2,3] row_mask:0xf bank_mask:0x8
	v_mov_b32_dpp v168, v176 quad_perm:[0,1,2,3] row_mask:0xf bank_mask:0xc
	v_mov_b32_dpp v169, v177 quad_perm:[0,1,2,3] row_mask:0xf bank_mask:0xc
	v_exp_f32_e32 v200, v168
	v_mov_b32_dpp v170, v178 quad_perm:[0,1,2,3] row_mask:0xf bank_mask:0xc
	v_exp_f32_e32 v201, v169
	v_mov_b32_dpp v179, v183 quad_perm:[0,1,2,3] row_mask:0xf bank_mask:0x8
	v_exp_f32_e32 v202, v170
	v_add_f32_e32 v200, 1.0, v200
	v_add_f32_e32 v201, 1.0, v201
	v_mov_b32_dpp v171, v179 quad_perm:[0,1,2,3] row_mask:0xf bank_mask:0xc
	v_add_f32_e32 v202, 1.0, v202
	v_rcp_f32_e32 v202, v202
	v_exp_f32_e32 v203, v171
	v_rcp_f32_e32 v200, v200
	v_rcp_f32_e32 v201, v201
	v_fmamk_f32 v204, v202, 0xc0b8aa3b, v222
	v_add_f32_e32 v203, 1.0, v203
	v_mul_f32_e32 v205, v200, v204
	v_rcp_f32_e32 v203, v203
	v_fma_f32 v220, v201, v220, v205
	v_exp_f32_e32 v206, v220
	v_mul_f32_e32 v207, -2.0, v203
	v_add_f32_e32 v206, 1.0, v206
	v_rcp_f32_e32 v206, v206
	s_nop 0
	v_fma_mixlo_f16 v208, v206, v207, v203
	ds_write_b16 v225, v208 offset:576
	ds_write_b128 v227, v[160:163] offset:0
	ds_read_b128 v[196:199], v226 offset:5440
	v_fma_f32 v215, v206, v207, v203
	v_mfma_f32_16x16x32_f16 v[164:167], v[64:67], v[128:131], v[116:119]
	v_mfma_f32_16x16x32_f16 v[164:167], v[68:71], v[132:135], v[164:167]
	s_waitcnt lgkmcnt(1)
	s_barrier
	ds_read_b128 v[184:187], v224 offset:576
	ds_read_b128 v[188:191], v224 offset:640
	v_mfma_f32_16x16x32_f16 v[164:167], v[72:75], v[136:139], v[164:167]
	v_mfma_f32_16x16x32_f16 v[164:167], v[76:79], v[140:143], v[164:167]
	s_waitcnt lgkmcnt(0)
	v_mfma_f32_16x16x32_f16 v[168:171], v[16:19], v[184:187], v[196:199]
	v_mfma_f32_16x16x32_f16 v[172:175], v[24:27], v[184:187], v[196:199]
	v_mfma_f32_16x16x32_f16 v[176:179], v[32:35], v[184:187], v[196:199]
	v_mfma_f32_16x16x32_f16 v[180:183], v[40:43], v[184:187], v[196:199]
	v_mfma_f32_16x16x32_f16 v[168:171], v[20:23], v[188:191], v[168:171]
	v_mfma_f32_16x16x32_f16 v[172:175], v[28:31], v[188:191], v[172:175]
	v_mfma_f32_16x16x32_f16 v[176:179], v[36:39], v[188:191], v[176:179]
	v_max_f32_e32 v221, v221, v215
	s_nop 5
	v_mov_b32_dpp v168, v172 quad_perm:[0,1,2,3] row_mask:0xf bank_mask:0x2
	v_mov_b32_dpp v169, v173 quad_perm:[0,1,2,3] row_mask:0xf bank_mask:0x2
	v_mfma_f32_16x16x32_f16 v[180:183], v[44:47], v[188:191], v[180:183]
	v_mov_b32_dpp v170, v174 quad_perm:[0,1,2,3] row_mask:0xf bank_mask:0x2
	v_mov_b32_dpp v171, v175 quad_perm:[0,1,2,3] row_mask:0xf bank_mask:0x2
	s_nop 5
	v_mov_b32_dpp v176, v180 quad_perm:[0,1,2,3] row_mask:0xf bank_mask:0x8
	v_mov_b32_dpp v177, v181 quad_perm:[0,1,2,3] row_mask:0xf bank_mask:0x8
	v_mov_b32_dpp v178, v182 quad_perm:[0,1,2,3] row_mask:0xf bank_mask:0x8
	v_mov_b32_dpp v168, v176 quad_perm:[0,1,2,3] row_mask:0xf bank_mask:0xc
	v_mov_b32_dpp v169, v177 quad_perm:[0,1,2,3] row_mask:0xf bank_mask:0xc
	v_exp_f32_e32 v200, v168
	v_mov_b32_dpp v170, v178 quad_perm:[0,1,2,3] row_mask:0xf bank_mask:0xc
	v_exp_f32_e32 v201, v169
	v_mov_b32_dpp v179, v183 quad_perm:[0,1,2,3] row_mask:0xf bank_mask:0x8
	v_exp_f32_e32 v202, v170
	v_add_f32_e32 v200, 1.0, v200
	v_add_f32_e32 v201, 1.0, v201
	v_mov_b32_dpp v171, v179 quad_perm:[0,1,2,3] row_mask:0xf bank_mask:0xc
	v_add_f32_e32 v202, 1.0, v202
	v_rcp_f32_e32 v202, v202
	v_exp_f32_e32 v203, v171
	v_rcp_f32_e32 v200, v200
	v_rcp_f32_e32 v201, v201
	v_fmamk_f32 v204, v202, 0xc0b8aa3b, v222
	v_add_f32_e32 v203, 1.0, v203
	v_mul_f32_e32 v205, v200, v204
	v_rcp_f32_e32 v203, v203
	v_fma_f32 v220, v201, v220, v205
	v_exp_f32_e32 v206, v220
	v_mul_f32_e32 v207, -2.0, v203
	v_add_f32_e32 v206, 1.0, v206
	v_rcp_f32_e32 v206, v206
	s_nop 0
	v_fma_mixlo_f16 v208, v206, v207, v203
	ds_write_b16 v225, v208 offset:0
	ds_write_b128 v227, v[164:167] offset:64
	ds_read_b128 v[192:195], v226 offset:6528
	v_fma_f32 v215, v206, v207, v203
	v_mfma_f32_16x16x32_f16 v[160:163], v[80:83], v[128:131], v[120:123]
	v_mfma_f32_16x16x32_f16 v[160:163], v[84:87], v[132:135], v[160:163]
	s_waitcnt lgkmcnt(1)
	s_barrier
	ds_read_b128 v[184:187], v224 offset:0
	ds_read_b128 v[188:191], v224 offset:64
	v_mfma_f32_16x16x32_f16 v[160:163], v[88:91], v[136:139], v[160:163]
	v_mfma_f32_16x16x32_f16 v[160:163], v[92:95], v[140:143], v[160:163]
	s_waitcnt lgkmcnt(0)
	v_mfma_f32_16x16x32_f16 v[168:171], v[16:19], v[184:187], v[192:195]
	v_mfma_f32_16x16x32_f16 v[172:175], v[24:27], v[184:187], v[192:195]
	v_mfma_f32_16x16x32_f16 v[176:179], v[32:35], v[184:187], v[192:195]
	v_mfma_f32_16x16x32_f16 v[180:183], v[40:43], v[184:187], v[192:195]
	v_mfma_f32_16x16x32_f16 v[168:171], v[20:23], v[188:191], v[168:171]
	v_mfma_f32_16x16x32_f16 v[172:175], v[28:31], v[188:191], v[172:175]
	v_mfma_f32_16x16x32_f16 v[176:179], v[36:39], v[188:191], v[176:179]
	v_max_f32_e32 v221, v221, v215
	s_nop 5
	v_mov_b32_dpp v168, v172 quad_perm:[0,1,2,3] row_mask:0xf bank_mask:0x2
	v_mov_b32_dpp v169, v173 quad_perm:[0,1,2,3] row_mask:0xf bank_mask:0x2
	v_mfma_f32_16x16x32_f16 v[180:183], v[44:47], v[188:191], v[180:183]
	v_mov_b32_dpp v170, v174 quad_perm:[0,1,2,3] row_mask:0xf bank_mask:0x2
	v_mov_b32_dpp v171, v175 quad_perm:[0,1,2,3] row_mask:0xf bank_mask:0x2
	s_nop 5
	v_mov_b32_dpp v176, v180 quad_perm:[0,1,2,3] row_mask:0xf bank_mask:0x8
	v_mov_b32_dpp v177, v181 quad_perm:[0,1,2,3] row_mask:0xf bank_mask:0x8
	v_mov_b32_dpp v178, v182 quad_perm:[0,1,2,3] row_mask:0xf bank_mask:0x8
	v_mov_b32_dpp v168, v176 quad_perm:[0,1,2,3] row_mask:0xf bank_mask:0xc
	v_mov_b32_dpp v169, v177 quad_perm:[0,1,2,3] row_mask:0xf bank_mask:0xc
	v_exp_f32_e32 v200, v168
	v_mov_b32_dpp v170, v178 quad_perm:[0,1,2,3] row_mask:0xf bank_mask:0xc
	v_exp_f32_e32 v201, v169
	v_mov_b32_dpp v179, v183 quad_perm:[0,1,2,3] row_mask:0xf bank_mask:0x8
	v_exp_f32_e32 v202, v170
	v_add_f32_e32 v200, 1.0, v200
	v_add_f32_e32 v201, 1.0, v201
	v_mov_b32_dpp v171, v179 quad_perm:[0,1,2,3] row_mask:0xf bank_mask:0xc
	v_add_f32_e32 v202, 1.0, v202
	v_rcp_f32_e32 v202, v202
	v_exp_f32_e32 v203, v171
	v_rcp_f32_e32 v200, v200
	v_rcp_f32_e32 v201, v201
	v_fmamk_f32 v204, v202, 0xc0b8aa3b, v222
	v_add_f32_e32 v203, 1.0, v203
	v_mul_f32_e32 v205, v200, v204
	v_rcp_f32_e32 v203, v203
	v_fma_f32 v220, v201, v220, v205
	v_exp_f32_e32 v206, v220
	v_mul_f32_e32 v207, -2.0, v203
	v_add_f32_e32 v206, 1.0, v206
	v_rcp_f32_e32 v206, v206
	s_nop 0
	v_fma_mixlo_f16 v208, v206, v207, v203
	ds_write_b16 v225, v208 offset:576
	ds_write_b128 v227, v[160:163] offset:128
	ds_read_b128 v[196:199], v226 offset:7616
	v_fma_f32 v215, v206, v207, v203
	v_mfma_f32_16x16x32_f16 v[164:167], v[96:99], v[128:131], v[124:127]
	v_mfma_f32_16x16x32_f16 v[164:167], v[100:103], v[132:135], v[164:167]
	s_waitcnt lgkmcnt(1)
	s_barrier
	ds_read_b128 v[184:187], v224 offset:576
	ds_read_b128 v[188:191], v224 offset:640
	v_mfma_f32_16x16x32_f16 v[164:167], v[104:107], v[136:139], v[164:167]
	v_mfma_f32_16x16x32_f16 v[164:167], v[108:111], v[140:143], v[164:167]
	s_waitcnt lgkmcnt(0)
	v_mfma_f32_16x16x32_f16 v[168:171], v[16:19], v[184:187], v[196:199]
	v_mfma_f32_16x16x32_f16 v[172:175], v[24:27], v[184:187], v[196:199]
	v_mfma_f32_16x16x32_f16 v[176:179], v[32:35], v[184:187], v[196:199]
	v_mfma_f32_16x16x32_f16 v[180:183], v[40:43], v[184:187], v[196:199]
	v_mfma_f32_16x16x32_f16 v[168:171], v[20:23], v[188:191], v[168:171]
	v_mfma_f32_16x16x32_f16 v[172:175], v[28:31], v[188:191], v[172:175]
	v_mfma_f32_16x16x32_f16 v[176:179], v[36:39], v[188:191], v[176:179]
	v_max_f32_e32 v221, v221, v215
	s_nop 5
	v_mov_b32_dpp v168, v172 quad_perm:[0,1,2,3] row_mask:0xf bank_mask:0x2
	v_mov_b32_dpp v169, v173 quad_perm:[0,1,2,3] row_mask:0xf bank_mask:0x2
	v_mfma_f32_16x16x32_f16 v[180:183], v[44:47], v[188:191], v[180:183]
	v_mov_b32_dpp v170, v174 quad_perm:[0,1,2,3] row_mask:0xf bank_mask:0x2
	v_mov_b32_dpp v171, v175 quad_perm:[0,1,2,3] row_mask:0xf bank_mask:0x2
	s_nop 5
	v_mov_b32_dpp v176, v180 quad_perm:[0,1,2,3] row_mask:0xf bank_mask:0x8
	v_mov_b32_dpp v177, v181 quad_perm:[0,1,2,3] row_mask:0xf bank_mask:0x8
	v_mov_b32_dpp v178, v182 quad_perm:[0,1,2,3] row_mask:0xf bank_mask:0x8
	v_mov_b32_dpp v168, v176 quad_perm:[0,1,2,3] row_mask:0xf bank_mask:0xc
	v_mov_b32_dpp v169, v177 quad_perm:[0,1,2,3] row_mask:0xf bank_mask:0xc
	v_exp_f32_e32 v200, v168
	v_mov_b32_dpp v170, v178 quad_perm:[0,1,2,3] row_mask:0xf bank_mask:0xc
	v_exp_f32_e32 v201, v169
	v_mov_b32_dpp v179, v183 quad_perm:[0,1,2,3] row_mask:0xf bank_mask:0x8
	v_exp_f32_e32 v202, v170
	v_add_f32_e32 v200, 1.0, v200
	v_add_f32_e32 v201, 1.0, v201
	v_mov_b32_dpp v171, v179 quad_perm:[0,1,2,3] row_mask:0xf bank_mask:0xc
	v_add_f32_e32 v202, 1.0, v202
	v_rcp_f32_e32 v202, v202
	v_exp_f32_e32 v203, v171
	v_rcp_f32_e32 v200, v200
	v_rcp_f32_e32 v201, v201
	v_fmamk_f32 v204, v202, 0xc0b8aa3b, v222
	v_add_f32_e32 v203, 1.0, v203
	v_mul_f32_e32 v205, v200, v204
	v_rcp_f32_e32 v203, v203
	v_fma_f32 v220, v201, v220, v205
	v_exp_f32_e32 v206, v220
	v_mul_f32_e32 v207, -2.0, v203
	v_add_f32_e32 v206, 1.0, v206
	v_rcp_f32_e32 v206, v206
	s_nop 0
	v_fma_mixlo_f16 v208, v206, v207, v203
	ds_write_b16 v225, v208 offset:0
	ds_write_b128 v227, v[164:167] offset:192
	ds_read_b128 v[192:195], v226 offset:0
	v_fma_f32 v215, v206, v207, v203
	s_waitcnt vmcnt(0)
	v_mfma_f32_16x16x32_f16 v[160:163], v[48:51], v[144:147], v[112:115]
	v_mfma_f32_16x16x32_f16 v[160:163], v[52:55], v[148:151], v[160:163]
	s_waitcnt lgkmcnt(1)
	s_barrier
	s_sub_u32 s4, s4, 1
	s_cmp_lg_u32 s4, 0
	s_cbranch_scc1 .Llstm3_loop
	v_max_f32_e32 v221, v221, v215
	global_store_dword v230, v221, s[12:13]
	s_endpgm
